# passCU: static s_setprio 1 for waves 4-7 before the edge loop
# speedup vs baseline: 1.0026x; 1.0026x over previous
	.amdhsa_kernel _Z4k_U2PKtPK15HIP_vector_typeIjLj4EEPKdPKfS8_S8_PtPd
		.amdhsa_group_segment_fixed_size 18944
		.amdhsa_private_segment_fixed_size 0
		.amdhsa_kernarg_size 320
		.amdhsa_user_sgpr_count 2
		.amdhsa_user_sgpr_dispatch_ptr 0
		.amdhsa_user_sgpr_queue_ptr 0
		.amdhsa_user_sgpr_kernarg_segment_ptr 1
		.amdhsa_user_sgpr_dispatch_id 0
		.amdhsa_user_sgpr_kernarg_preload_length 0
		.amdhsa_user_sgpr_kernarg_preload_offset 0
		.amdhsa_user_sgpr_private_segment_size 0
		.amdhsa_uses_dynamic_stack 0
		.amdhsa_enable_private_segment 0
		.amdhsa_system_sgpr_workgroup_id_x 1
		.amdhsa_system_sgpr_workgroup_id_y 0
		.amdhsa_system_sgpr_workgroup_id_z 0
		.amdhsa_system_sgpr_workgroup_info 0
		.amdhsa_system_vgpr_workitem_id 0
		.amdhsa_next_free_vgpr 104
		.amdhsa_next_free_sgpr 28
		.amdhsa_accum_offset 72
		.amdhsa_reserve_vcc 1
		.amdhsa_float_round_mode_32 0
		.amdhsa_float_round_mode_16_64 0
		.amdhsa_float_denorm_mode_32 3
		.amdhsa_float_denorm_mode_16_64 3
		.amdhsa_dx10_clamp 1
		.amdhsa_ieee_mode 1
		.amdhsa_fp16_overflow 0
		.amdhsa_tg_split 0
		.amdhsa_exception_fp_ieee_invalid_op 0
		.amdhsa_exception_fp_denorm_src 0
		.amdhsa_exception_fp_ieee_div_zero 0
		.amdhsa_exception_fp_ieee_overflow 0
		.amdhsa_exception_fp_ieee_underflow 0
		.amdhsa_exception_fp_ieee_inexact 0
		.amdhsa_exception_int_div_zero 0
	.end_amdhsa_kernel

.LBB8_4:
	s_load_dwordx2 s[12:13], s[0:1], 0xa8
	s_load_dwordx2 s[18:19], s[0:1], 0x98
	s_waitcnt lgkmcnt(0)
	s_sub_i32 s4, s28, s20
	s_add_i32 s4, s4, 31
	v_and_b32_e32 v1, 63, v0
	s_ashr_i32 s15, s4, 5
	s_cmp_lt_i32 s15, 1
	v_add_u32_e32 v90, s14, v98
	v_and_b32_e32 v100, 32, v0
	v_lshlrev_b32_e32 v99, 4, v1
	s_cbranch_scc1 .LBB8_7
	s_load_dwordx8 s[4:11], s[0:1], 0x0
	s_load_dwordx2 s[24:25], s[0:1], 0x20
	s_load_dwordx2 s[30:31], s[0:1], 0x80
	s_load_dwordx2 s[48:49], s[0:1], 0x90
	v_and_b32_e32 v34, 7, v1
	v_lshlrev_b32_e32 v34, 4, v34
	v_lshrrev_b32_e32 v35, 3, v1
	s_lshl_b32 s32, s3, 12
	s_add_i32 s33, s32, 0x2000
	s_add_i32 s32, s32, 0xb500
	s_cmp_lt_u32 s3, 2
	s_cselect_b32 s32, s33, s32
	v_lshlrev_b32_e32 v36, 1, v35
	v_and_b32_e32 v36, 7, v36
	v_or_b32_e32 v37, 1, v36
	v_lshlrev_b32_e32 v36, 4, v36
	v_lshlrev_b32_e32 v37, 4, v37
	v_xor_b32_e32 v36, v36, v34
	v_xor_b32_e32 v37, v37, v34
	v_lshl_add_u32 v39, v35, 9, s32
	v_add_u32_e32 v36, v36, v39
	v_add_u32_e32 v37, v37, v39
	v_lshrrev_b32_e32 v38, 1, v98
	v_and_b32_e32 v38, 7, v38
	v_lshrrev_b32_e32 v39, 3, v100
	v_xor_b32_e32 v38, v38, v39
	v_lshlrev_b32_e32 v38, 4, v38
	v_lshl_add_u32 v39, v98, 7, s32
	v_add_u32_e32 v38, v38, v39
	v_lshlrev_b32_e32 v35, 4, v35
	s_mov_b32 s35, 0x1869f
	v_mov_b32_e32 v2, 0
	v_mov_b32_e32 v3, 0
	v_mov_b32_e32 v4, 0
	v_mov_b32_e32 v5, 0
	v_mov_b32_e32 v6, 0
	v_mov_b32_e32 v7, 0
	v_mov_b32_e32 v8, 0
	v_mov_b32_e32 v9, 0
	v_mov_b32_e32 v10, 0
	v_mov_b32_e32 v11, 0
	v_mov_b32_e32 v12, 0
	v_mov_b32_e32 v13, 0
	v_mov_b32_e32 v14, 0
	v_mov_b32_e32 v15, 0
	v_mov_b32_e32 v16, 0
	v_mov_b32_e32 v17, 0
	v_mov_b32_e32 v18, 0
	v_mov_b32_e32 v19, 0
	v_mov_b32_e32 v20, 0
	v_mov_b32_e32 v21, 0
	v_mov_b32_e32 v22, 0
	v_mov_b32_e32 v23, 0
	v_mov_b32_e32 v24, 0
	v_mov_b32_e32 v25, 0
	v_mov_b32_e32 v26, 0
	v_mov_b32_e32 v27, 0
	v_mov_b32_e32 v28, 0
	v_mov_b32_e32 v29, 0
	v_mov_b32_e32 v30, 0
	v_mov_b32_e32 v31, 0
	v_mov_b32_e32 v32, 0
	v_mov_b32_e32 v33, 0
	s_waitcnt vmcnt(0) lgkmcnt(0)
	v_mov_b32_e32 v42, v70
	v_mov_b32_e32 v43, v71
	v_mov_b32_e32 v44, v72
	v_mov_b32_e32 v45, v73
	v_mov_b32_e32 v46, v74
	v_mov_b32_e32 v47, v75
	v_mov_b32_e32 v48, v76
	v_mov_b32_e32 v49, v77
	v_mov_b32_e32 v50, v78
	v_mov_b32_e32 v51, v79
	v_mov_b32_e32 v52, v80
	v_mov_b32_e32 v53, v81
	v_lshlrev_b32_e32 v39, 2, v90
	global_load_dword v40, v39, s[30:31]
	global_load_dword v41, v39, s[30:31] offset:4
	s_lshl_b32 s34, s20, 2
	v_min_u32_e32 v42, s35, v42
	v_min_u32_e32 v46, s35, v46
	v_min_u32_e32 v43, s35, v43
	v_min_u32_e32 v47, s35, v47
	v_min_u32_e32 v44, s35, v44
	v_min_u32_e32 v48, s35, v48
	v_min_u32_e32 v45, s35, v45
	v_min_u32_e32 v49, s35, v49
	v_lshl_or_b32 v42, v42, 7, v34
	v_lshl_or_b32 v46, v46, 7, v34
	v_lshl_or_b32 v43, v43, 7, v34
	v_lshl_or_b32 v47, v47, 7, v34
	v_lshl_or_b32 v44, v44, 7, v34
	v_lshl_or_b32 v48, v48, 7, v34
	v_lshl_or_b32 v45, v45, 7, v34
	v_lshl_or_b32 v49, v49, 7, v34
	global_load_dwordx4 v[70:73], v42, s[24:25]
	global_load_dwordx4 v[74:77], v43, s[24:25]
	global_load_dwordx4 v[78:81], v44, s[24:25]
	global_load_dwordx4 v[82:85], v45, s[24:25]
	global_load_dwordx4 v[86:89], v46, s[10:11]
	global_load_dwordx4 v[90:93], v47, s[10:11]
	global_load_dwordx4 v[94:97], v48, s[10:11]
	global_load_dwordx4 v[102:105], v49, s[10:11]
	s_add_i32 s34, s34, 0x80
	v_add_u32_e32 v39, s34, v35
	global_load_dwordx4 v[42:45], v39, s[4:5]
	global_load_dwordx4 v[46:49], v39, s[6:7]
	s_cmp_lt_u32 s3, 4
	s_cbranch_scc1 .Lcu_nopri
	s_setprio 1
.Lcu_nopri:
	v_lshlrev_b32_e32 v39, 1, v34
	ds_read_b128 v[112:115], v39 offset:53248
	ds_read_b128 v[116:119], v39 offset:53760
	ds_read_b128 v[120:123], v39 offset:53504

amdhsa.kernels:
  - .agpr_count:     0
    .args:
      - .actual_access:  read_only
        .address_space:  global
        .offset:         0
        .size:           8
        .value_kind:     global_buffer
      - .actual_access:  read_only
        .address_space:  global
        .offset:         8
        .size:           8
        .value_kind:     global_buffer
      - .actual_access:  read_only
        .address_space:  global
        .offset:         16
        .size:           8
        .value_kind:     global_buffer
      - .actual_access:  read_only
        .address_space:  global
        .offset:         24
        .size:           8
        .value_kind:     global_buffer
      - .actual_access:  write_only
        .address_space:  global
        .offset:         32
        .size:           8
        .value_kind:     global_buffer
      - .actual_access:  write_only
        .address_space:  global
        .offset:         40
        .size:           8
        .value_kind:     global_buffer
      - .actual_access:  write_only
        .address_space:  global
        .offset:         48
        .size:           8
        .value_kind:     global_buffer
      - .offset:         56
        .size:           4
        .value_kind:     hidden_block_count_x
      - .offset:         60
        .size:           4
        .value_kind:     hidden_block_count_y
      - .offset:         64
        .size:           4
        .value_kind:     hidden_block_count_z
      - .offset:         68
        .size:           2
        .value_kind:     hidden_group_size_x
      - .offset:         70
        .size:           2
        .value_kind:     hidden_group_size_y
      - .offset:         72
        .size:           2
        .value_kind:     hidden_group_size_z
      - .offset:         74
        .size:           2
        .value_kind:     hidden_remainder_x
      - .offset:         76
        .size:           2
        .value_kind:     hidden_remainder_y
      - .offset:         78
        .size:           2
        .value_kind:     hidden_remainder_z
      - .offset:         96
        .size:           8
        .value_kind:     hidden_global_offset_x
      - .offset:         104
        .size:           8
        .value_kind:     hidden_global_offset_y
      - .offset:         112
        .size:           8
        .value_kind:     hidden_global_offset_z
      - .offset:         120
        .size:           2
        .value_kind:     hidden_grid_dims
    .group_segment_fixed_size: 0
    .kernarg_segment_align: 8
    .kernarg_segment_size: 312
    .language:       OpenCL C
    .language_version:
      - 2
      - 0
    .max_flat_workgroup_size: 256
    .name:           _Z6k_prepPKfS0_S0_S0_P15HIP_vector_typeIjLj4EEPiPd
    .private_segment_fixed_size: 0
    .sgpr_count:     25
    .sgpr_spill_count: 0
    .symbol:         _Z6k_prepPKfS0_S0_S0_P15HIP_vector_typeIjLj4EEPiPd.kd
    .uniform_work_group_size: 1
    .uses_dynamic_stack: false
    .vgpr_count:     24
    .vgpr_spill_count: 0
    .wavefront_size: 64
  - .agpr_count:     0
    .args:
      - .actual_access:  read_only
        .address_space:  global
        .offset:         0
        .size:           8
        .value_kind:     global_buffer
      - .actual_access:  read_only
        .address_space:  global
        .offset:         8
        .size:           8
        .value_kind:     global_buffer
      - .actual_access:  read_only
        .address_space:  global
        .offset:         16
        .size:           8
        .value_kind:     global_buffer
      - .actual_access:  read_only
        .address_space:  global
        .offset:         24
        .size:           8
        .value_kind:     global_buffer
      - .actual_access:  read_only
        .address_space:  global
        .offset:         32
        .size:           8
        .value_kind:     global_buffer
      - .actual_access:  write_only
        .address_space:  global
        .offset:         40
        .size:           8
        .value_kind:     global_buffer
      - .actual_access:  write_only
        .address_space:  global
        .offset:         48
        .size:           8
        .value_kind:     global_buffer
    .group_segment_fixed_size: 4112
    .kernarg_segment_align: 8
    .kernarg_segment_size: 56
    .language:       OpenCL C
    .language_version:
      - 2
      - 0
    .max_flat_workgroup_size: 256
    .name:           _Z10k_bscatterPKiS0_PKfS0_S0_PiP15HIP_vector_typeIjLj2EE
    .private_segment_fixed_size: 0
    .sgpr_count:     28
    .sgpr_spill_count: 0
    .symbol:         _Z10k_bscatterPKiS0_PKfS0_S0_PiP15HIP_vector_typeIjLj2EE.kd
    .uniform_work_group_size: 1
    .uses_dynamic_stack: false
    .vgpr_count:     78
    .vgpr_spill_count: 0
    .wavefront_size: 64
  - .agpr_count:     0
    .args:
      - .actual_access:  read_only
        .address_space:  global
        .offset:         0
        .size:           8
        .value_kind:     global_buffer
      - .actual_access:  read_only
        .address_space:  global
        .offset:         8
        .size:           8
        .value_kind:     global_buffer
      - .actual_access:  write_only
        .address_space:  global
        .offset:         16
        .size:           8
        .value_kind:     global_buffer
      - .actual_access:  write_only
        .address_space:  global
        .offset:         24
        .size:           8
        .value_kind:     global_buffer
      - .actual_access:  write_only
        .address_space:  global
        .offset:         32
        .size:           8
        .value_kind:     global_buffer
      - .actual_access:  write_only
        .address_space:  global
        .offset:         40
        .size:           8
        .value_kind:     global_buffer
    .group_segment_fixed_size: 29200
    .kernarg_segment_align: 8
    .kernarg_segment_size: 48
    .language:       OpenCL C
    .language_version:
      - 2
      - 0
    .max_flat_workgroup_size: 256
    .name:           _Z7k_bsortPKiPK15HIP_vector_typeIjLj2EEPiS5_S5_Pf
    .private_segment_fixed_size: 0
    .sgpr_count:     106
    .sgpr_spill_count: 12
    .symbol:         _Z7k_bsortPKiPK15HIP_vector_typeIjLj2EEPiS5_S5_Pf.kd
    .uniform_work_group_size: 1
    .uses_dynamic_stack: false
    .vgpr_count:     69
    .vgpr_spill_count: 0
    .wavefront_size: 64
  - .agpr_count:     32
    .args:
      - .address_space:  global
        .offset:         0
        .size:           8
        .value_kind:     global_buffer
      - .actual_access:  read_only
        .address_space:  global
        .offset:         8
        .size:           8
        .value_kind:     global_buffer
      - .actual_access:  read_only
        .address_space:  global
        .offset:         16
        .size:           8
        .value_kind:     global_buffer
      - .actual_access:  read_only
        .address_space:  global
        .offset:         24
        .size:           8
        .value_kind:     global_buffer
      - .actual_access:  read_only
        .address_space:  global
        .offset:         32
        .size:           8
        .value_kind:     global_buffer
      - .actual_access:  read_only
        .address_space:  global
        .offset:         40
        .size:           8
        .value_kind:     global_buffer
      - .address_space:  global
        .offset:         48
        .size:           8
        .value_kind:     global_buffer
      - .address_space:  global
        .offset:         56
        .size:           8
        .value_kind:     global_buffer
      - .offset:         64
        .size:           4
        .value_kind:     hidden_block_count_x
      - .offset:         68
        .size:           4
        .value_kind:     hidden_block_count_y
      - .offset:         72
        .size:           4
        .value_kind:     hidden_block_count_z
      - .offset:         76
        .size:           2
        .value_kind:     hidden_group_size_x
      - .offset:         78
        .size:           2
        .value_kind:     hidden_group_size_y
      - .offset:         80
        .size:           2
        .value_kind:     hidden_group_size_z
      - .offset:         82
        .size:           2
        .value_kind:     hidden_remainder_x
      - .offset:         84
        .size:           2
        .value_kind:     hidden_remainder_y
      - .offset:         86
        .size:           2
        .value_kind:     hidden_remainder_z
      - .offset:         104
        .size:           8
        .value_kind:     hidden_global_offset_x
      - .offset:         112
        .size:           8
        .value_kind:     hidden_global_offset_y
      - .offset:         120
        .size:           8
        .value_kind:     hidden_global_offset_z
      - .offset:         128
        .size:           2
        .value_kind:     hidden_grid_dims
    .group_segment_fixed_size: 18944
    .kernarg_segment_align: 8
    .kernarg_segment_size: 320
    .language:       OpenCL C
    .language_version:
      - 2
      - 0
    .max_flat_workgroup_size: 256
    .name:           _Z4k_U2PKtPK15HIP_vector_typeIjLj4EEPKdPKfS8_S8_PtPd
    .private_segment_fixed_size: 0
    .sgpr_count:     34
    .sgpr_spill_count: 0
    .symbol:         _Z4k_U2PKtPK15HIP_vector_typeIjLj4EEPKdPKfS8_S8_PtPd.kd
    .uniform_work_group_size: 1
    .uses_dynamic_stack: false
    .vgpr_count:     104
    .vgpr_spill_count: 0
    .wavefront_size: 64
  - .agpr_count:     0
    .args:
      - .actual_access:  read_only
        .address_space:  global
        .offset:         0
        .size:           8
        .value_kind:     global_buffer
      - .actual_access:  read_only
        .address_space:  global
        .offset:         8
        .size:           8
        .value_kind:     global_buffer
      - .actual_access:  write_only
        .address_space:  global
        .offset:         16
        .size:           8
        .value_kind:     global_buffer
    .group_segment_fixed_size: 0
    .kernarg_segment_align: 8
    .kernarg_segment_size: 24
    .language:       OpenCL C
    .language_version:
      - 2
      - 0
    .max_flat_workgroup_size: 1024
    .name:           _Z7k_finalPKdPKfPf
    .private_segment_fixed_size: 0
    .sgpr_count:     28
    .sgpr_spill_count: 0
    .symbol:         _Z7k_finalPKdPKfPf.kd
    .uniform_work_group_size: 1
    .uses_dynamic_stack: false
    .vgpr_count:     10
    .vgpr_spill_count: 0
    .wavefront_size: 64
  - .agpr_count:     64
    .args:
      - .actual_access:  read_only
        .address_space:  global
        .offset:         0
        .size:           8
        .value_kind:     global_buffer
      - .address_space:  global
        .offset:         8
        .size:           8
        .value_kind:     global_buffer
      - .actual_access:  write_only
        .address_space:  global
        .offset:         16
        .size:           8
        .value_kind:     global_buffer
      - .actual_access:  read_only
        .address_space:  global
        .offset:         24
        .size:           8
        .value_kind:     global_buffer
      - .actual_access:  read_only
        .address_space:  global
        .offset:         32
        .size:           8
        .value_kind:     global_buffer
      - .actual_access:  read_only
        .address_space:  global
        .offset:         40
        .size:           8
        .value_kind:     global_buffer
      - .actual_access:  read_only
        .address_space:  global
        .offset:         48
        .size:           8
        .value_kind:     global_buffer
      - .actual_access:  read_only
        .address_space:  global
        .offset:         56
        .size:           8
        .value_kind:     global_buffer
      - .actual_access:  write_only
        .address_space:  global
        .offset:         64
        .size:           8
        .value_kind:     global_buffer
      - .actual_access:  write_only
        .address_space:  global
        .offset:         72
        .size:           8
        .value_kind:     global_buffer
      - .actual_access:  write_only
        .address_space:  global
        .offset:         80
        .size:           8
        .value_kind:     global_buffer
      - .offset:         88
        .size:           4
        .value_kind:     hidden_block_count_x
      - .offset:         92
        .size:           4
        .value_kind:     hidden_block_count_y
      - .offset:         96
        .size:           4
        .value_kind:     hidden_block_count_z
      - .offset:         100
        .size:           2
        .value_kind:     hidden_group_size_x
      - .offset:         102
        .size:           2
        .value_kind:     hidden_group_size_y
      - .offset:         104
        .size:           2
        .value_kind:     hidden_group_size_z
      - .offset:         106
        .size:           2
        .value_kind:     hidden_remainder_x
      - .offset:         108
        .size:           2
        .value_kind:     hidden_remainder_y
      - .offset:         110
        .size:           2
        .value_kind:     hidden_remainder_z
      - .offset:         128
        .size:           8
        .value_kind:     hidden_global_offset_x
      - .offset:         136
        .size:           8
        .value_kind:     hidden_global_offset_y
      - .offset:         144
        .size:           8
        .value_kind:     hidden_global_offset_z
      - .offset:         152
        .size:           2
        .value_kind:     hidden_grid_dims
    .group_segment_fixed_size: 45312
    .kernarg_segment_align: 8
    .kernarg_segment_size: 344
    .language:       OpenCL C
    .language_version:
      - 2
      - 0
    .max_flat_workgroup_size: 256
    .name:           _Z14k_bcount_node0ItEvPKiPiS2_PKfS4_S4_S4_PK15HIP_vector_typeIjLj4EEPtPT_SB_
    .private_segment_fixed_size: 0
    .sgpr_count:     26
    .sgpr_spill_count: 0
    .symbol:         _Z14k_bcount_node0ItEvPKiPiS2_PKfS4_S4_S4_PK15HIP_vector_typeIjLj4EEPtPT_SB_.kd
    .uniform_work_group_size: 1
    .uses_dynamic_stack: false
    .vgpr_count:     232
    .vgpr_spill_count: 0
    .wavefront_size: 64
  - .agpr_count:     0
    .args:
      - .actual_access:  read_only
        .address_space:  global
        .offset:         0
        .size:           8
        .value_kind:     global_buffer
      - .actual_access:  read_only
        .address_space:  global
        .offset:         8
        .size:           8
        .value_kind:     global_buffer
      - .actual_access:  read_only
        .address_space:  global
        .offset:         16
        .size:           8
        .value_kind:     global_buffer
      - .actual_access:  read_only
        .address_space:  global
        .offset:         24
        .size:           8
        .value_kind:     global_buffer
      - .actual_access:  read_only
        .address_space:  global
        .offset:         32
        .size:           8
        .value_kind:     global_buffer
      - .actual_access:  read_only
        .address_space:  global
        .offset:         40
        .size:           8
        .value_kind:     global_buffer
      - .address_space:  global
        .offset:         48
        .size:           8
        .value_kind:     global_buffer
      - .offset:         56
        .size:           4
        .value_kind:     hidden_block_count_x
      - .offset:         60
        .size:           4
        .value_kind:     hidden_block_count_y
      - .offset:         64
        .size:           4
        .value_kind:     hidden_block_count_z
      - .offset:         68
        .size:           2
        .value_kind:     hidden_group_size_x
      - .offset:         70
        .size:           2
        .value_kind:     hidden_group_size_y
      - .offset:         72
        .size:           2
        .value_kind:     hidden_group_size_z
      - .offset:         74
        .size:           2
        .value_kind:     hidden_remainder_x
      - .offset:         76
        .size:           2
        .value_kind:     hidden_remainder_y
      - .offset:         78
        .size:           2
        .value_kind:     hidden_remainder_z
      - .offset:         96
        .size:           8
        .value_kind:     hidden_global_offset_x
      - .offset:         104
        .size:           8
        .value_kind:     hidden_global_offset_y
      - .offset:         112
        .size:           8
        .value_kind:     hidden_global_offset_z
      - .offset:         120
        .size:           2
        .value_kind:     hidden_grid_dims
    .group_segment_fixed_size: 2048
    .kernarg_segment_align: 8
    .kernarg_segment_size: 312
    .language:       OpenCL C
    .language_version:
      - 2
      - 0
    .max_flat_workgroup_size: 256
    .name:           _Z7k_passAItEvPKiS1_PKfPKT_S6_S3_Pd
    .private_segment_fixed_size: 0
    .sgpr_count:     36
    .sgpr_spill_count: 0
    .symbol:         _Z7k_passAItEvPKiS1_PKfPKT_S6_S3_Pd.kd
    .uniform_work_group_size: 1
    .uses_dynamic_stack: false
    .vgpr_count:     104
    .vgpr_spill_count: 0
    .wavefront_size: 64
  - .agpr_count:     0
    .args:
      - .actual_access:  read_only
        .address_space:  global
        .offset:         0
        .size:           8
        .value_kind:     global_buffer
      - .actual_access:  read_only
        .address_space:  global
        .offset:         8
        .size:           8
        .value_kind:     global_buffer
      - .actual_access:  read_only
        .address_space:  global
        .offset:         16
        .size:           8
        .value_kind:     global_buffer
      - .actual_access:  read_only
        .address_space:  global
        .offset:         24
        .size:           8
        .value_kind:     global_buffer
      - .actual_access:  read_only
        .address_space:  global
        .offset:         32
        .size:           8
        .value_kind:     global_buffer
      - .actual_access:  read_only
        .address_space:  global
        .offset:         40
        .size:           8
        .value_kind:     global_buffer
      - .actual_access:  read_only
        .address_space:  global
        .offset:         48
        .size:           8
        .value_kind:     global_buffer
      - .actual_access:  read_only
        .address_space:  global
        .offset:         56
        .size:           8
        .value_kind:     global_buffer
      - .actual_access:  read_only
        .address_space:  global
        .offset:         64
        .size:           8
        .value_kind:     global_buffer
      - .actual_access:  read_only
        .address_space:  global
        .offset:         72
        .size:           8
        .value_kind:     global_buffer
      - .actual_access:  read_only
        .address_space:  global
        .offset:         80
        .size:           8
        .value_kind:     global_buffer
      - .actual_access:  read_only
        .address_space:  global
        .offset:         88
        .size:           8
        .value_kind:     global_buffer
      - .actual_access:  read_only
        .address_space:  global
        .offset:         96
        .size:           8
        .value_kind:     global_buffer
      - .address_space:  global
        .offset:         104
        .size:           8
        .value_kind:     global_buffer
      - .actual_access:  read_only
        .address_space:  global
        .offset:         112
        .size:           8
        .value_kind:     global_buffer
      - .actual_access:  read_only
        .address_space:  global
        .offset:         120
        .size:           8
        .value_kind:     global_buffer
      - .address_space:  global
        .offset:         128
        .size:           8
        .value_kind:     global_buffer
      - .offset:         136
        .size:           4
        .value_kind:     hidden_block_count_x
      - .offset:         140
        .size:           4
        .value_kind:     hidden_block_count_y
      - .offset:         144
        .size:           4
        .value_kind:     hidden_block_count_z
      - .offset:         148
        .size:           2
        .value_kind:     hidden_group_size_x
      - .offset:         150
        .size:           2
        .value_kind:     hidden_group_size_y
      - .offset:         152
        .size:           2
        .value_kind:     hidden_group_size_z
      - .offset:         154
        .size:           2
        .value_kind:     hidden_remainder_x
      - .offset:         156
        .size:           2
        .value_kind:     hidden_remainder_y
      - .offset:         158
        .size:           2
        .value_kind:     hidden_remainder_z
      - .offset:         176
        .size:           8
        .value_kind:     hidden_global_offset_x
      - .offset:         184
        .size:           8
        .value_kind:     hidden_global_offset_y
      - .offset:         192
        .size:           8
        .value_kind:     hidden_global_offset_z
      - .offset:         200
        .size:           2
        .value_kind:     hidden_grid_dims
    .group_segment_fixed_size: 37632
    .kernarg_segment_align: 8
    .kernarg_segment_size: 392
    .language:       OpenCL C
    .language_version:
      - 2
      - 0
    .max_flat_workgroup_size: 256
    .name:           _Z7k_passLILi1ELi0ELi1EEvPKiS1_PKfPKtS5_S3_S3_S3_S3_S3_S3_PK15HIP_vector_typeIjLj4EEPKdPdS1_PtS1_
    .private_segment_fixed_size: 0
    .sgpr_count:     62
    .sgpr_spill_count: 0
    .symbol:         _Z7k_passLILi1ELi0ELi1EEvPKiS1_PKfPKtS5_S3_S3_S3_S3_S3_S3_PK15HIP_vector_typeIjLj4EEPKdPdS1_PtS1_.kd
    .uniform_work_group_size: 1
    .uses_dynamic_stack: false
    .vgpr_count:     128
    .vgpr_spill_count: 0
    .wavefront_size: 64
  - .agpr_count:     0
    .args:
      - .actual_access:  read_only
        .address_space:  global
        .offset:         0
        .size:           8
        .value_kind:     global_buffer
      - .actual_access:  read_only
        .address_space:  global
        .offset:         8
        .size:           8
        .value_kind:     global_buffer
      - .actual_access:  read_only
        .address_space:  global
        .offset:         16
        .size:           8
        .value_kind:     global_buffer
      - .actual_access:  read_only
        .address_space:  global
        .offset:         24
        .size:           8
        .value_kind:     global_buffer
      - .actual_access:  read_only
        .address_space:  global
        .offset:         32
        .size:           8
        .value_kind:     global_buffer
      - .actual_access:  read_only
        .address_space:  global
        .offset:         40
        .size:           8
        .value_kind:     global_buffer
      - .actual_access:  read_only
        .address_space:  global
        .offset:         48
        .size:           8
        .value_kind:     global_buffer
      - .actual_access:  read_only
        .address_space:  global
        .offset:         56
        .size:           8
        .value_kind:     global_buffer
      - .actual_access:  read_only
        .address_space:  global
        .offset:         64
        .size:           8
        .value_kind:     global_buffer
      - .actual_access:  read_only
        .address_space:  global
        .offset:         72
        .size:           8
        .value_kind:     global_buffer
      - .actual_access:  read_only
        .address_space:  global
        .offset:         80
        .size:           8
        .value_kind:     global_buffer
      - .actual_access:  read_only
        .address_space:  global
        .offset:         88
        .size:           8
        .value_kind:     global_buffer
      - .actual_access:  read_only
        .address_space:  global
        .offset:         96
        .size:           8
        .value_kind:     global_buffer
      - .actual_access:  read_only
        .address_space:  global
        .offset:         104
        .size:           8
        .value_kind:     global_buffer
      - .actual_access:  read_only
        .address_space:  global
        .offset:         112
        .size:           8
        .value_kind:     global_buffer
      - .actual_access:  read_only
        .address_space:  global
        .offset:         120
        .size:           8
        .value_kind:     global_buffer
      - .actual_access:  read_only
        .address_space:  global
        .offset:         128
        .size:           8
        .value_kind:     global_buffer
      - .address_space:  global
        .offset:         136
        .size:           8
        .value_kind:     global_buffer
      - .actual_access:  read_only
        .address_space:  global
        .offset:         144
        .size:           8
        .value_kind:     global_buffer
      - .actual_access:  read_only
        .address_space:  global
        .offset:         152
        .size:           8
        .value_kind:     global_buffer
      - .actual_access:  write_only
        .address_space:  global
        .offset:         160
        .size:           8
        .value_kind:     global_buffer
      - .address_space:  global
        .offset:         168
        .size:           8
        .value_kind:     global_buffer
      - .offset:         176
        .size:           4
        .value_kind:     hidden_block_count_x
      - .offset:         180
        .size:           4
        .value_kind:     hidden_block_count_y
      - .offset:         184
        .size:           4
        .value_kind:     hidden_block_count_z
      - .offset:         188
        .size:           2
        .value_kind:     hidden_group_size_x
      - .offset:         190
        .size:           2
        .value_kind:     hidden_group_size_y
      - .offset:         192
        .size:           2
        .value_kind:     hidden_group_size_z
      - .offset:         194
        .size:           2
        .value_kind:     hidden_remainder_x
      - .offset:         196
        .size:           2
        .value_kind:     hidden_remainder_y
      - .offset:         198
        .size:           2
        .value_kind:     hidden_remainder_z
      - .offset:         216
        .size:           8
        .value_kind:     hidden_global_offset_x
      - .offset:         224
        .size:           8
        .value_kind:     hidden_global_offset_y
      - .offset:         232
        .size:           8
        .value_kind:     hidden_global_offset_z
      - .offset:         240
        .size:           2
        .value_kind:     hidden_grid_dims
    .group_segment_fixed_size: 79104
    .kernarg_segment_align: 8
    .kernarg_segment_size: 432
    .language:       OpenCL C
    .language_version:
      - 2
      - 0
    .max_flat_workgroup_size: 512
    .name:           _Z8k_passCUILi1EEvPKiS1_PKfPKtS5_S3_S3_S3_S3_S3_S3_PK15HIP_vector_typeIjLj4EES9_S9_PKdSB_S1_S1_S5_S3_PtPd
    .private_segment_fixed_size: 0
    .sgpr_count:     35
    .sgpr_spill_count: 0
    .symbol:         _Z8k_passCUILi1EEvPKiS1_PKfPKtS5_S3_S3_S3_S3_S3_S3_PK15HIP_vector_typeIjLj4EES9_S9_PKdSB_S1_S1_S5_S3_PtPd.kd
    .uniform_work_group_size: 1
    .uses_dynamic_stack: false
    .vgpr_count:     128
    .vgpr_spill_count: 0
    .wavefront_size: 64
  - .agpr_count:     64
    .args:
      - .actual_access:  read_only
        .address_space:  global
        .offset:         0
        .size:           8
        .value_kind:     global_buffer
      - .address_space:  global
        .offset:         8
        .size:           8
        .value_kind:     global_buffer
      - .actual_access:  read_only
        .address_space:  global
        .offset:         16
        .size:           8
        .value_kind:     global_buffer
      - .actual_access:  read_only
        .address_space:  global
        .offset:         24
        .size:           8
        .value_kind:     global_buffer
      - .actual_access:  read_only
        .address_space:  global
        .offset:         32
        .size:           8
        .value_kind:     global_buffer
      - .actual_access:  read_only
        .address_space:  global
        .offset:         40
        .size:           8
        .value_kind:     global_buffer
      - .actual_access:  read_only
        .address_space:  global
        .offset:         48
        .size:           8
        .value_kind:     global_buffer
      - .actual_access:  write_only
        .address_space:  global
        .offset:         56
        .size:           8
        .value_kind:     global_buffer
      - .actual_access:  write_only
        .address_space:  global
        .offset:         64
        .size:           8
        .value_kind:     global_buffer
      - .actual_access:  read_only
        .address_space:  global
        .offset:         72
        .size:           8
        .value_kind:     global_buffer
      - .actual_access:  read_only
        .address_space:  global
        .offset:         80
        .size:           8
        .value_kind:     global_buffer
      - .offset:         88
        .size:           4
        .value_kind:     hidden_block_count_x
      - .offset:         92
        .size:           4
        .value_kind:     hidden_block_count_y
      - .offset:         96
        .size:           4
        .value_kind:     hidden_block_count_z
      - .offset:         100
        .size:           2
        .value_kind:     hidden_group_size_x
      - .offset:         102
        .size:           2
        .value_kind:     hidden_group_size_y
      - .offset:         104
        .size:           2
        .value_kind:     hidden_group_size_z
      - .offset:         106
        .size:           2
        .value_kind:     hidden_remainder_x
      - .offset:         108
        .size:           2
        .value_kind:     hidden_remainder_y
      - .offset:         110
        .size:           2
        .value_kind:     hidden_remainder_z
      - .offset:         128
        .size:           8
        .value_kind:     hidden_global_offset_x
      - .offset:         136
        .size:           8
        .value_kind:     hidden_global_offset_y
      - .offset:         144
        .size:           8
        .value_kind:     hidden_global_offset_z
      - .offset:         152
        .size:           2
        .value_kind:     hidden_grid_dims
    .group_segment_fixed_size: 33280
    .kernarg_segment_align: 8
    .kernarg_segment_size: 344
    .language:       OpenCL C
    .language_version:
      - 2
      - 0
    .max_flat_workgroup_size: 256
    .name:           _Z4k_U3ILb0EtEvPKtPtPKdPKfS6_PK15HIP_vector_typeIjLj4EES6_PT0_SC_S6_Pd
    .private_segment_fixed_size: 0
    .sgpr_count:     20
    .sgpr_spill_count: 0
    .symbol:         _Z4k_U3ILb0EtEvPKtPtPKdPKfS6_PK15HIP_vector_typeIjLj4EES6_PT0_SC_S6_Pd.kd
    .uniform_work_group_size: 1
    .uses_dynamic_stack: false
    .vgpr_count:     144
    .vgpr_spill_count: 0
    .wavefront_size: 64
  - .agpr_count:     0
    .args:
      - .actual_access:  read_only
        .address_space:  global
        .offset:         0
        .size:           8
        .value_kind:     global_buffer
      - .actual_access:  read_only
        .address_space:  global
        .offset:         8
        .size:           8
        .value_kind:     global_buffer
      - .actual_access:  read_only
        .address_space:  global
        .offset:         16
        .size:           8
        .value_kind:     global_buffer
      - .actual_access:  read_only
        .address_space:  global
        .offset:         24
        .size:           8
        .value_kind:     global_buffer
      - .actual_access:  read_only
        .address_space:  global
        .offset:         32
        .size:           8
        .value_kind:     global_buffer
      - .actual_access:  read_only
        .address_space:  global
        .offset:         40
        .size:           8
        .value_kind:     global_buffer
      - .actual_access:  read_only
        .address_space:  global
        .offset:         48
        .size:           8
        .value_kind:     global_buffer
      - .actual_access:  read_only
        .address_space:  global
        .offset:         56
        .size:           8
        .value_kind:     global_buffer
      - .actual_access:  read_only
        .address_space:  global
        .offset:         64
        .size:           8
        .value_kind:     global_buffer
      - .actual_access:  read_only
        .address_space:  global
        .offset:         72
        .size:           8
        .value_kind:     global_buffer
      - .address_space:  global
        .offset:         80
        .size:           8
        .value_kind:     global_buffer
      - .offset:         88
        .size:           4
        .value_kind:     hidden_block_count_x
      - .offset:         92
        .size:           4
        .value_kind:     hidden_block_count_y
      - .offset:         96
        .size:           4
        .value_kind:     hidden_block_count_z
      - .offset:         100
        .size:           2
        .value_kind:     hidden_group_size_x
      - .offset:         102
        .size:           2
        .value_kind:     hidden_group_size_y
      - .offset:         104
        .size:           2
        .value_kind:     hidden_group_size_z
      - .offset:         106
        .size:           2
        .value_kind:     hidden_remainder_x
      - .offset:         108
        .size:           2
        .value_kind:     hidden_remainder_y
      - .offset:         110
        .size:           2
        .value_kind:     hidden_remainder_z
      - .offset:         128
        .size:           8
        .value_kind:     hidden_global_offset_x
      - .offset:         136
        .size:           8
        .value_kind:     hidden_global_offset_y
      - .offset:         144
        .size:           8
        .value_kind:     hidden_global_offset_z
      - .offset:         152
        .size:           2
        .value_kind:     hidden_grid_dims
    .group_segment_fixed_size: 784
    .kernarg_segment_align: 8
    .kernarg_segment_size: 344
    .language:       OpenCL C
    .language_version:
      - 2
      - 0
    .max_flat_workgroup_size: 256
    .name:           _Z4k_U3ILb1EtEvPKtPtPKdPKfS6_PK15HIP_vector_typeIjLj4EES6_PT0_SC_S6_Pd
    .private_segment_fixed_size: 0
    .sgpr_count:     20
    .sgpr_spill_count: 0
    .symbol:         _Z4k_U3ILb1EtEvPKtPtPKdPKfS6_PK15HIP_vector_typeIjLj4EES6_PT0_SC_S6_Pd.kd
    .uniform_work_group_size: 1
    .uses_dynamic_stack: false
    .vgpr_count:     79
    .vgpr_spill_count: 0
    .wavefront_size: 64
